# baseline (speedup 1.0000x reference)
_Z6k_normILb1EEvPKDF16_PKdPKfS5_Pvm:
	s_cmpk_gt_u32 s2, 0x30d
	s_cselect_b64 s[8:9], -1, 0
	s_load_dwordx2 s[18:19], s[0:1], 0x0
	s_cselect_b32 s38, 0x30e, 0
	s_cselect_b32 s39, 0x186a000, 0
	s_sub_i32 s38, s2, s38
	s_lshl_b32 s38, s38, 6
	s_load_dwordx4 s[4:7], s[0:1], 0x8
	s_load_dwordx2 s[10:11], s[0:1], 0x18
	s_and_b64 s[12:13], s[8:9], exec
	s_cselect_b32 s3, 0x1000, 0
	v_or_b32_e32 v1, s3, v0
	v_lshlrev_b32_e32 v1, 3, v1
	v_or_b32_e32 v10, 0x1000, v1
	s_waitcnt lgkmcnt(0)
	v_and_b32_e32 v62, 63, v0
	v_lshlrev_b32_e32 v62, 3, v62
	v_add_u32_e32 v62, s39, v62
	v_lshrrev_b32_e32 v63, 6, v0
	v_add_u32_e32 v63, s38, v63
	v_min_i32_e32 v46, 0xc34f, v63
	v_lshl_add_u32 v46, v46, 9, v62
	global_load_dwordx2 v[46:47], v46, s[18:19]
	v_add_u32_e32 v48, 4, v63
	v_min_i32_e32 v48, 0xc34f, v48
	v_lshl_add_u32 v48, v48, 9, v62
	global_load_dwordx2 v[48:49], v48, s[18:19]
	v_add_u32_e32 v50, 8, v63
	v_min_i32_e32 v50, 0xc34f, v50
	v_lshl_add_u32 v50, v50, 9, v62
	global_load_dwordx2 v[50:51], v50, s[18:19]
	v_add_u32_e32 v52, 12, v63
	v_min_i32_e32 v52, 0xc34f, v52
	v_lshl_add_u32 v52, v52, 9, v62
	global_load_dwordx2 v[52:53], v52, s[18:19]
	v_add_u32_e32 v54, 16, v63
	v_min_i32_e32 v54, 0xc34f, v54
	v_lshl_add_u32 v54, v54, 9, v62
	global_load_dwordx2 v[54:55], v54, s[18:19]
	v_add_u32_e32 v56, 20, v63
	v_min_i32_e32 v56, 0xc34f, v56
	v_lshl_add_u32 v56, v56, 9, v62
	global_load_dwordx2 v[56:57], v56, s[18:19]
	v_add_u32_e32 v58, 24, v63
	v_min_i32_e32 v58, 0xc34f, v58
	v_lshl_add_u32 v58, v58, 9, v62
	global_load_dwordx2 v[58:59], v58, s[18:19]
	v_add_u32_e32 v60, 28, v63
	v_min_i32_e32 v60, 0xc34f, v60
	v_lshl_add_u32 v60, v60, 9, v62
	global_load_dwordx2 v[60:61], v60, s[18:19]
	global_load_dwordx2 v[2:3], v1, s[4:5]
	global_load_dwordx2 v[4:5], v1, s[4:5] offset:2048
	global_load_dwordx2 v[6:7], v10, s[4:5]
	global_load_dwordx2 v[8:9], v10, s[4:5] offset:2048
	v_or_b32_e32 v18, 0x2000, v1
	v_or_b32_e32 v19, 0x3000, v1
	global_load_dwordx2 v[10:11], v18, s[4:5]
	global_load_dwordx2 v[12:13], v18, s[4:5] offset:2048
	global_load_dwordx2 v[14:15], v19, s[4:5]
	global_load_dwordx2 v[16:17], v19, s[4:5] offset:2048
	v_or_b32_e32 v26, 0x4000, v1
	v_or_b32_e32 v27, 0x5000, v1
	global_load_dwordx2 v[18:19], v26, s[4:5]
	global_load_dwordx2 v[20:21], v26, s[4:5] offset:2048
	global_load_dwordx2 v[22:23], v27, s[4:5]
	global_load_dwordx2 v[24:25], v27, s[4:5] offset:2048
	v_or_b32_e32 v34, 0x6000, v1
	v_or_b32_e32 v1, 0x7000, v1
	global_load_dwordx2 v[26:27], v34, s[4:5]
	global_load_dwordx2 v[28:29], v34, s[4:5] offset:2048
	global_load_dwordx2 v[30:31], v1, s[4:5]
	global_load_dwordx2 v[32:33], v1, s[4:5] offset:2048
	s_cselect_b32 s3, 0x100, 0
	v_or_b32_e32 v1, s3, v0
	v_lshlrev_b32_e32 v1, 2, v1
	global_load_dword v34, v1, s[6:7]
	global_load_dword v35, v1, s[10:11]
	s_mov_b32 s10, 0
	s_cselect_b32 s3, 0x3fffcf2, 0
	s_mov_b32 s11, 0x40e86a00
	s_add_i32 s3, s3, s2
	s_lshl_b32 s4, s3, 6
	s_mov_b32 s5, 0x800000
	v_lshrrev_b32_e32 v1, 5, v0
	s_add_i32 s12, s4, 64
	s_min_i32 s16, s12, 0xc350
	s_mov_b64 s[6:7], 0
	v_lshlrev_b32_e32 v36, 2, v0
	s_waitcnt vmcnt(17)
	v_add_f64 v[2:3], v[2:3], 0
	s_waitcnt vmcnt(16)
	v_add_f64 v[4:5], v[4:5], 0
	s_waitcnt vmcnt(15)
	v_add_f64 v[2:3], v[2:3], v[6:7]
	s_waitcnt vmcnt(14)
	v_add_f64 v[4:5], v[4:5], v[8:9]
	s_waitcnt vmcnt(13)
	v_add_f64 v[2:3], v[2:3], v[10:11]
	s_waitcnt vmcnt(12)
	v_add_f64 v[4:5], v[4:5], v[12:13]
	s_waitcnt vmcnt(11)
	v_add_f64 v[2:3], v[2:3], v[14:15]
	s_waitcnt vmcnt(10)
	v_add_f64 v[4:5], v[4:5], v[16:17]
	s_waitcnt vmcnt(9)
	v_add_f64 v[2:3], v[2:3], v[18:19]
	s_waitcnt vmcnt(8)
	v_add_f64 v[4:5], v[4:5], v[20:21]
	s_waitcnt vmcnt(7)
	v_add_f64 v[2:3], v[2:3], v[22:23]
	s_waitcnt vmcnt(6)
	v_add_f64 v[4:5], v[4:5], v[24:25]
	s_waitcnt vmcnt(5)
	v_add_f64 v[2:3], v[2:3], v[26:27]
	s_waitcnt vmcnt(4)
	v_add_f64 v[4:5], v[4:5], v[28:29]
	s_waitcnt vmcnt(3)
	v_add_f64 v[2:3], v[2:3], v[30:31]
	s_waitcnt vmcnt(2)
	v_add_f64 v[4:5], v[4:5], v[32:33]
	v_div_scale_f64 v[6:7], s[2:3], s[10:11], s[10:11], v[2:3]
	v_div_scale_f64 v[10:11], s[2:3], s[10:11], s[10:11], v[4:5]
	v_rcp_f64_e32 v[12:13], v[6:7]
	v_rcp_f64_e32 v[14:15], v[10:11]
	v_div_scale_f64 v[8:9], vcc, v[2:3], s[10:11], v[2:3]
	v_fma_f64 v[18:19], -v[6:7], v[12:13], 1.0
	v_fma_f64 v[20:21], -v[10:11], v[14:15], 1.0
	v_fmac_f64_e32 v[12:13], v[12:13], v[18:19]
	v_fmac_f64_e32 v[14:15], v[14:15], v[20:21]
	v_fma_f64 v[18:19], -v[6:7], v[12:13], 1.0
	v_fma_f64 v[20:21], -v[10:11], v[14:15], 1.0
	v_fmac_f64_e32 v[12:13], v[12:13], v[18:19]
	v_div_scale_f64 v[16:17], s[2:3], v[4:5], s[10:11], v[4:5]
	v_fmac_f64_e32 v[14:15], v[14:15], v[20:21]
	v_mul_f64 v[18:19], v[8:9], v[12:13]
	v_mul_f64 v[20:21], v[16:17], v[14:15]
	v_fma_f64 v[6:7], -v[6:7], v[18:19], v[8:9]
	v_fma_f64 v[8:9], -v[10:11], v[20:21], v[16:17]
	v_div_fmas_f64 v[6:7], v[6:7], v[12:13], v[18:19]
	s_mov_b64 vcc, s[2:3]
	v_div_fixup_f64 v[2:3], v[6:7], s[10:11], v[2:3]
	v_div_fmas_f64 v[6:7], v[8:9], v[14:15], v[20:21]
	v_div_fixup_f64 v[4:5], v[6:7], s[10:11], v[4:5]
	v_fma_f64 v[4:5], -v[2:3], v[2:3], v[4:5]
	v_cmp_ngt_f64_e32 vcc, 0, v[4:5]
	v_cvt_f32_f64_e32 v2, v[2:3]
	v_or_b32_e32 v18, s4, v1
	v_cndmask_b32_e32 v5, 0, v5, vcc
	v_cndmask_b32_e32 v4, 0, v4, vcc
	v_cvt_f32_f64_e32 v4, v[4:5]
	v_add_f32_e32 v4, 0x3727c5ac, v4
	v_mul_f32_e32 v5, 0x4b800000, v4
	v_cmp_gt_f32_e32 vcc, s5, v4
	s_nop 1
	v_cndmask_b32_e32 v4, v4, v5, vcc
	v_rsq_f32_e32 v4, v4
	s_nop 0
	v_mul_f32_e32 v3, 0x45800000, v4
	v_cndmask_b32_e32 v3, v4, v3, vcc
	s_waitcnt vmcnt(1)
	v_mul_f32_e32 v3, v3, v34
	s_waitcnt vmcnt(0)
	v_fma_f32 v2, -v3, v2, v35
	v_cmp_gt_i32_e32 vcc, s16, v18
	ds_write2st64_b32 v36, v3, v2 offset1:4
	s_waitcnt lgkmcnt(0)
	s_barrier
	s_load_dwordx4 s[12:15], s[0:1], 0x20
	s_and_b64 s[0:1], s[8:9], exec
	s_cselect_b32 s0, 0x186a000, 0
	v_and_b32_e32 v10, 63, v0
	v_lshrrev_b32_e32 v11, 6, v0
	v_lshlrev_b32_e32 v12, 4, v10
	ds_read_b128 v[2:5], v12
	ds_read_b128 v[6:9], v12 offset:1024
	v_lshlrev_b32_e32 v10, 3, v10
	v_readfirstlane_b32 s23, v11
	s_mov_b32 s28, 0x3c23d70a
	s_waitcnt lgkmcnt(0)
	s_add_u32 s2, s18, s0
	s_addc_u32 s3, s19, 0
	s_and_b64 s[20:21], s[8:9], exec
	s_cselect_b32 s21, s15, 0
	s_cselect_b32 s20, s14, 0
	s_lshl_b64 s[20:21], s[20:21], 2
	s_add_u32 s12, s12, s20
	s_addc_u32 s13, s13, s21
	s_add_i32 s23, s23, s4
	s_add_i32 s22, s23, 32
	s_min_i32 s22, s22, 0xc34f
	s_lshl_b32 s22, s22, 9
	s_add_u32 s24, s2, s22
	s_addc_u32 s25, s3, 0
	global_load_dwordx2 v[14:15], v10, s[24:25]
	s_add_i32 s22, s23, 36
	s_min_i32 s22, s22, 0xc34f
	s_lshl_b32 s22, s22, 9
	s_add_u32 s24, s2, s22
	s_addc_u32 s25, s3, 0
	global_load_dwordx2 v[16:17], v10, s[24:25]
	s_add_i32 s22, s23, 40
	s_min_i32 s22, s22, 0xc34f
	s_lshl_b32 s22, s22, 9
	s_add_u32 s24, s2, s22
	s_addc_u32 s25, s3, 0
	global_load_dwordx2 v[18:19], v10, s[24:25]
	s_add_i32 s22, s23, 44
	s_min_i32 s22, s22, 0xc34f
	s_lshl_b32 s22, s22, 9
	s_add_u32 s24, s2, s22
	s_addc_u32 s25, s3, 0
	global_load_dwordx2 v[20:21], v10, s[24:25]
	s_add_i32 s22, s23, 48
	s_min_i32 s22, s22, 0xc34f
	s_lshl_b32 s22, s22, 9
	s_add_u32 s24, s2, s22
	s_addc_u32 s25, s3, 0
	global_load_dwordx2 v[22:23], v10, s[24:25]
	s_add_i32 s22, s23, 52
	s_min_i32 s22, s22, 0xc34f
	s_lshl_b32 s22, s22, 9
	s_add_u32 s24, s2, s22
	s_addc_u32 s25, s3, 0
	global_load_dwordx2 v[24:25], v10, s[24:25]
	s_add_i32 s22, s23, 56
	s_min_i32 s22, s22, 0xc34f
	s_lshl_b32 s22, s22, 9
	s_add_u32 s24, s2, s22
	s_addc_u32 s25, s3, 0
	global_load_dwordx2 v[26:27], v10, s[24:25]
	s_add_i32 s22, s23, 60
	s_min_i32 s22, s22, 0xc34f
	s_lshl_b32 s22, s22, 9
	s_add_u32 s24, s2, s22
	s_addc_u32 s25, s3, 0
	global_load_dwordx2 v[28:29], v10, s[24:25]
	v_cvt_f32_f16_sdwa v33, v46 dst_sel:DWORD dst_unused:UNUSED_PAD src0_sel:WORD_1
	v_cvt_f32_f16_e32 v32, v46
	v_cvt_f32_f16_sdwa v35, v47 dst_sel:DWORD dst_unused:UNUSED_PAD src0_sel:WORD_1
	v_cvt_f32_f16_e32 v34, v47
	v_pk_fma_f32 v[32:33], v[2:3], v[32:33], v[6:7]
	v_pk_fma_f32 v[34:35], v[4:5], v[34:35], v[8:9]
	v_pk_mul_f32 v[36:37], v[32:33], s[28:29] op_sel_hi:[1,0]
	v_pk_mul_f32 v[38:39], v[34:35], s[28:29] op_sel_hi:[1,0]
	v_cmp_lt_f32_e64 s[30:31], 0, v32
	v_cmp_lt_f32_e64 s[32:33], 0, v33
	v_cmp_lt_f32_e64 s[34:35], 0, v34
	v_cmp_lt_f32_e64 s[36:37], 0, v35
	v_cndmask_b32_e64 v32, v36, v32, s[30:31]
	v_cndmask_b32_e64 v33, v37, v33, s[32:33]
	v_cndmask_b32_e64 v34, v38, v34, s[34:35]
	v_cndmask_b32_e64 v35, v39, v35, s[36:37]
	s_add_i32 s22, s23, 0
	s_cmp_lt_i32 s22, s16
	s_cbranch_scc0 .Ln1_skip_0
	s_lshl_b32 s22, s22, 10
	s_add_u32 s26, s12, s22
	s_addc_u32 s27, s13, 0
	global_store_dwordx4 v12, v[32:35], s[26:27] sc1
.Ln1_skip_0:
	v_cvt_f32_f16_sdwa v41, v48 dst_sel:DWORD dst_unused:UNUSED_PAD src0_sel:WORD_1
	v_cvt_f32_f16_e32 v40, v48
	v_cvt_f32_f16_sdwa v43, v49 dst_sel:DWORD dst_unused:UNUSED_PAD src0_sel:WORD_1
	v_cvt_f32_f16_e32 v42, v49
	v_pk_fma_f32 v[40:41], v[2:3], v[40:41], v[6:7]
	v_pk_fma_f32 v[42:43], v[4:5], v[42:43], v[8:9]
	v_pk_mul_f32 v[44:45], v[40:41], s[28:29] op_sel_hi:[1,0]
	v_pk_mul_f32 v[46:47], v[42:43], s[28:29] op_sel_hi:[1,0]
	v_cmp_lt_f32_e64 s[30:31], 0, v40
	v_cmp_lt_f32_e64 s[32:33], 0, v41
	v_cmp_lt_f32_e64 s[34:35], 0, v42
	v_cmp_lt_f32_e64 s[36:37], 0, v43
	v_cndmask_b32_e64 v40, v44, v40, s[30:31]
	v_cndmask_b32_e64 v41, v45, v41, s[32:33]
	v_cndmask_b32_e64 v42, v46, v42, s[34:35]
	v_cndmask_b32_e64 v43, v47, v43, s[36:37]
	s_add_i32 s22, s23, 4
	s_cmp_lt_i32 s22, s16
	s_cbranch_scc0 .Ln1_skip_1
	s_lshl_b32 s22, s22, 10
	s_add_u32 s26, s12, s22
	s_addc_u32 s27, s13, 0
	global_store_dwordx4 v12, v[40:43], s[26:27] sc1
.Ln1_skip_1:
	v_cvt_f32_f16_sdwa v33, v50 dst_sel:DWORD dst_unused:UNUSED_PAD src0_sel:WORD_1
	v_cvt_f32_f16_e32 v32, v50
	v_cvt_f32_f16_sdwa v35, v51 dst_sel:DWORD dst_unused:UNUSED_PAD src0_sel:WORD_1
	v_cvt_f32_f16_e32 v34, v51
	v_pk_fma_f32 v[32:33], v[2:3], v[32:33], v[6:7]
	v_pk_fma_f32 v[34:35], v[4:5], v[34:35], v[8:9]
	v_pk_mul_f32 v[36:37], v[32:33], s[28:29] op_sel_hi:[1,0]
	v_pk_mul_f32 v[38:39], v[34:35], s[28:29] op_sel_hi:[1,0]
	v_cmp_lt_f32_e64 s[30:31], 0, v32
	v_cmp_lt_f32_e64 s[32:33], 0, v33
	v_cmp_lt_f32_e64 s[34:35], 0, v34
	v_cmp_lt_f32_e64 s[36:37], 0, v35
	v_cndmask_b32_e64 v32, v36, v32, s[30:31]
	v_cndmask_b32_e64 v33, v37, v33, s[32:33]
	v_cndmask_b32_e64 v34, v38, v34, s[34:35]
	v_cndmask_b32_e64 v35, v39, v35, s[36:37]
	s_add_i32 s22, s23, 8
	s_cmp_lt_i32 s22, s16
	s_cbranch_scc0 .Ln1_skip_2
	s_lshl_b32 s22, s22, 10
	s_add_u32 s26, s12, s22
	s_addc_u32 s27, s13, 0
	global_store_dwordx4 v12, v[32:35], s[26:27] sc1
.Ln1_skip_2:
	v_cvt_f32_f16_sdwa v41, v52 dst_sel:DWORD dst_unused:UNUSED_PAD src0_sel:WORD_1
	v_cvt_f32_f16_e32 v40, v52
	v_cvt_f32_f16_sdwa v43, v53 dst_sel:DWORD dst_unused:UNUSED_PAD src0_sel:WORD_1
	v_cvt_f32_f16_e32 v42, v53
	v_pk_fma_f32 v[40:41], v[2:3], v[40:41], v[6:7]
	v_pk_fma_f32 v[42:43], v[4:5], v[42:43], v[8:9]
	v_pk_mul_f32 v[44:45], v[40:41], s[28:29] op_sel_hi:[1,0]
	v_pk_mul_f32 v[46:47], v[42:43], s[28:29] op_sel_hi:[1,0]
	v_cmp_lt_f32_e64 s[30:31], 0, v40
	v_cmp_lt_f32_e64 s[32:33], 0, v41
	v_cmp_lt_f32_e64 s[34:35], 0, v42
	v_cmp_lt_f32_e64 s[36:37], 0, v43
	v_cndmask_b32_e64 v40, v44, v40, s[30:31]
	v_cndmask_b32_e64 v41, v45, v41, s[32:33]
	v_cndmask_b32_e64 v42, v46, v42, s[34:35]
	v_cndmask_b32_e64 v43, v47, v43, s[36:37]
	s_add_i32 s22, s23, 12
	s_cmp_lt_i32 s22, s16
	s_cbranch_scc0 .Ln1_skip_3
	s_lshl_b32 s22, s22, 10
	s_add_u32 s26, s12, s22
	s_addc_u32 s27, s13, 0
	global_store_dwordx4 v12, v[40:43], s[26:27] sc1
.Ln1_skip_3:
	v_cvt_f32_f16_sdwa v33, v54 dst_sel:DWORD dst_unused:UNUSED_PAD src0_sel:WORD_1
	v_cvt_f32_f16_e32 v32, v54
	v_cvt_f32_f16_sdwa v35, v55 dst_sel:DWORD dst_unused:UNUSED_PAD src0_sel:WORD_1
	v_cvt_f32_f16_e32 v34, v55
	v_pk_fma_f32 v[32:33], v[2:3], v[32:33], v[6:7]
	v_pk_fma_f32 v[34:35], v[4:5], v[34:35], v[8:9]
	v_pk_mul_f32 v[36:37], v[32:33], s[28:29] op_sel_hi:[1,0]
	v_pk_mul_f32 v[38:39], v[34:35], s[28:29] op_sel_hi:[1,0]
	v_cmp_lt_f32_e64 s[30:31], 0, v32
	v_cmp_lt_f32_e64 s[32:33], 0, v33
	v_cmp_lt_f32_e64 s[34:35], 0, v34
	v_cmp_lt_f32_e64 s[36:37], 0, v35
	v_cndmask_b32_e64 v32, v36, v32, s[30:31]
	v_cndmask_b32_e64 v33, v37, v33, s[32:33]
	v_cndmask_b32_e64 v34, v38, v34, s[34:35]
	v_cndmask_b32_e64 v35, v39, v35, s[36:37]
	s_add_i32 s22, s23, 16
	s_cmp_lt_i32 s22, s16
	s_cbranch_scc0 .Ln1_skip_4
	s_lshl_b32 s22, s22, 10
	s_add_u32 s26, s12, s22
	s_addc_u32 s27, s13, 0
	global_store_dwordx4 v12, v[32:35], s[26:27] sc1
.Ln1_skip_4:
	v_cvt_f32_f16_sdwa v41, v56 dst_sel:DWORD dst_unused:UNUSED_PAD src0_sel:WORD_1
	v_cvt_f32_f16_e32 v40, v56
	v_cvt_f32_f16_sdwa v43, v57 dst_sel:DWORD dst_unused:UNUSED_PAD src0_sel:WORD_1
	v_cvt_f32_f16_e32 v42, v57
	v_pk_fma_f32 v[40:41], v[2:3], v[40:41], v[6:7]
	v_pk_fma_f32 v[42:43], v[4:5], v[42:43], v[8:9]
	v_pk_mul_f32 v[44:45], v[40:41], s[28:29] op_sel_hi:[1,0]
	v_pk_mul_f32 v[46:47], v[42:43], s[28:29] op_sel_hi:[1,0]
	v_cmp_lt_f32_e64 s[30:31], 0, v40
	v_cmp_lt_f32_e64 s[32:33], 0, v41
	v_cmp_lt_f32_e64 s[34:35], 0, v42
	v_cmp_lt_f32_e64 s[36:37], 0, v43
	v_cndmask_b32_e64 v40, v44, v40, s[30:31]
	v_cndmask_b32_e64 v41, v45, v41, s[32:33]
	v_cndmask_b32_e64 v42, v46, v42, s[34:35]
	v_cndmask_b32_e64 v43, v47, v43, s[36:37]
	s_add_i32 s22, s23, 20
	s_cmp_lt_i32 s22, s16
	s_cbranch_scc0 .Ln1_skip_5
	s_lshl_b32 s22, s22, 10
	s_add_u32 s26, s12, s22
	s_addc_u32 s27, s13, 0
	global_store_dwordx4 v12, v[40:43], s[26:27] sc1
.Ln1_skip_5:
	v_cvt_f32_f16_sdwa v33, v58 dst_sel:DWORD dst_unused:UNUSED_PAD src0_sel:WORD_1
	v_cvt_f32_f16_e32 v32, v58
	v_cvt_f32_f16_sdwa v35, v59 dst_sel:DWORD dst_unused:UNUSED_PAD src0_sel:WORD_1
	v_cvt_f32_f16_e32 v34, v59
	v_pk_fma_f32 v[32:33], v[2:3], v[32:33], v[6:7]
	v_pk_fma_f32 v[34:35], v[4:5], v[34:35], v[8:9]
	v_pk_mul_f32 v[36:37], v[32:33], s[28:29] op_sel_hi:[1,0]
	v_pk_mul_f32 v[38:39], v[34:35], s[28:29] op_sel_hi:[1,0]
	v_cmp_lt_f32_e64 s[30:31], 0, v32
	v_cmp_lt_f32_e64 s[32:33], 0, v33
	v_cmp_lt_f32_e64 s[34:35], 0, v34
	v_cmp_lt_f32_e64 s[36:37], 0, v35
	v_cndmask_b32_e64 v32, v36, v32, s[30:31]
	v_cndmask_b32_e64 v33, v37, v33, s[32:33]
	v_cndmask_b32_e64 v34, v38, v34, s[34:35]
	v_cndmask_b32_e64 v35, v39, v35, s[36:37]
	s_add_i32 s22, s23, 24
	s_cmp_lt_i32 s22, s16
	s_cbranch_scc0 .Ln1_skip_6
	s_lshl_b32 s22, s22, 10
	s_add_u32 s26, s12, s22
	s_addc_u32 s27, s13, 0
	global_store_dwordx4 v12, v[32:35], s[26:27] sc1
.Ln1_skip_6:
	v_cvt_f32_f16_sdwa v41, v60 dst_sel:DWORD dst_unused:UNUSED_PAD src0_sel:WORD_1
	v_cvt_f32_f16_e32 v40, v60
	v_cvt_f32_f16_sdwa v43, v61 dst_sel:DWORD dst_unused:UNUSED_PAD src0_sel:WORD_1
	v_cvt_f32_f16_e32 v42, v61
	v_pk_fma_f32 v[40:41], v[2:3], v[40:41], v[6:7]
	v_pk_fma_f32 v[42:43], v[4:5], v[42:43], v[8:9]
	v_pk_mul_f32 v[44:45], v[40:41], s[28:29] op_sel_hi:[1,0]
	v_pk_mul_f32 v[46:47], v[42:43], s[28:29] op_sel_hi:[1,0]
	v_cmp_lt_f32_e64 s[30:31], 0, v40
	v_cmp_lt_f32_e64 s[32:33], 0, v41
	v_cmp_lt_f32_e64 s[34:35], 0, v42
	v_cmp_lt_f32_e64 s[36:37], 0, v43
	v_cndmask_b32_e64 v40, v44, v40, s[30:31]
	v_cndmask_b32_e64 v41, v45, v41, s[32:33]
	v_cndmask_b32_e64 v42, v46, v42, s[34:35]
	v_cndmask_b32_e64 v43, v47, v43, s[36:37]
	s_add_i32 s22, s23, 28
	s_cmp_lt_i32 s22, s16
	s_cbranch_scc0 .Ln1_skip_7
	s_lshl_b32 s22, s22, 10
	s_add_u32 s26, s12, s22
	s_addc_u32 s27, s13, 0
	global_store_dwordx4 v12, v[40:43], s[26:27] sc1
.Ln1_skip_7:
	s_waitcnt vmcnt(15)
	v_cvt_f32_f16_sdwa v33, v14 dst_sel:DWORD dst_unused:UNUSED_PAD src0_sel:WORD_1
	v_cvt_f32_f16_e32 v32, v14
	v_cvt_f32_f16_sdwa v35, v15 dst_sel:DWORD dst_unused:UNUSED_PAD src0_sel:WORD_1
	v_cvt_f32_f16_e32 v34, v15
	v_pk_fma_f32 v[32:33], v[2:3], v[32:33], v[6:7]
	v_pk_fma_f32 v[34:35], v[4:5], v[34:35], v[8:9]
	v_pk_mul_f32 v[36:37], v[32:33], s[28:29] op_sel_hi:[1,0]
	v_pk_mul_f32 v[38:39], v[34:35], s[28:29] op_sel_hi:[1,0]
	v_cmp_lt_f32_e64 s[30:31], 0, v32
	v_cmp_lt_f32_e64 s[32:33], 0, v33
	v_cmp_lt_f32_e64 s[34:35], 0, v34
	v_cmp_lt_f32_e64 s[36:37], 0, v35
	v_cndmask_b32_e64 v32, v36, v32, s[30:31]
	v_cndmask_b32_e64 v33, v37, v33, s[32:33]
	v_cndmask_b32_e64 v34, v38, v34, s[34:35]
	v_cndmask_b32_e64 v35, v39, v35, s[36:37]
	s_add_i32 s22, s23, 32
	s_cmp_lt_i32 s22, s16
	s_cbranch_scc0 .Ln1_skip_8
	s_lshl_b32 s22, s22, 10
	s_add_u32 s26, s12, s22
	s_addc_u32 s27, s13, 0
	global_store_dwordx4 v12, v[32:35], s[26:27] sc1
.Ln1_skip_8:
	s_waitcnt vmcnt(15)
	v_cvt_f32_f16_sdwa v41, v16 dst_sel:DWORD dst_unused:UNUSED_PAD src0_sel:WORD_1
	v_cvt_f32_f16_e32 v40, v16
	v_cvt_f32_f16_sdwa v43, v17 dst_sel:DWORD dst_unused:UNUSED_PAD src0_sel:WORD_1
	v_cvt_f32_f16_e32 v42, v17
	v_pk_fma_f32 v[40:41], v[2:3], v[40:41], v[6:7]
	v_pk_fma_f32 v[42:43], v[4:5], v[42:43], v[8:9]
	v_pk_mul_f32 v[44:45], v[40:41], s[28:29] op_sel_hi:[1,0]
	v_pk_mul_f32 v[46:47], v[42:43], s[28:29] op_sel_hi:[1,0]
	v_cmp_lt_f32_e64 s[30:31], 0, v40
	v_cmp_lt_f32_e64 s[32:33], 0, v41
	v_cmp_lt_f32_e64 s[34:35], 0, v42
	v_cmp_lt_f32_e64 s[36:37], 0, v43
	v_cndmask_b32_e64 v40, v44, v40, s[30:31]
	v_cndmask_b32_e64 v41, v45, v41, s[32:33]
	v_cndmask_b32_e64 v42, v46, v42, s[34:35]
	v_cndmask_b32_e64 v43, v47, v43, s[36:37]
	s_add_i32 s22, s23, 36
	s_cmp_lt_i32 s22, s16
	s_cbranch_scc0 .Ln1_skip_9
	s_lshl_b32 s22, s22, 10
	s_add_u32 s26, s12, s22
	s_addc_u32 s27, s13, 0
	global_store_dwordx4 v12, v[40:43], s[26:27] sc1
.Ln1_skip_9:
	s_waitcnt vmcnt(15)
	v_cvt_f32_f16_sdwa v33, v18 dst_sel:DWORD dst_unused:UNUSED_PAD src0_sel:WORD_1
	v_cvt_f32_f16_e32 v32, v18
	v_cvt_f32_f16_sdwa v35, v19 dst_sel:DWORD dst_unused:UNUSED_PAD src0_sel:WORD_1
	v_cvt_f32_f16_e32 v34, v19
	v_pk_fma_f32 v[32:33], v[2:3], v[32:33], v[6:7]
	v_pk_fma_f32 v[34:35], v[4:5], v[34:35], v[8:9]
	v_pk_mul_f32 v[36:37], v[32:33], s[28:29] op_sel_hi:[1,0]
	v_pk_mul_f32 v[38:39], v[34:35], s[28:29] op_sel_hi:[1,0]
	v_cmp_lt_f32_e64 s[30:31], 0, v32
	v_cmp_lt_f32_e64 s[32:33], 0, v33
	v_cmp_lt_f32_e64 s[34:35], 0, v34
	v_cmp_lt_f32_e64 s[36:37], 0, v35
	v_cndmask_b32_e64 v32, v36, v32, s[30:31]
	v_cndmask_b32_e64 v33, v37, v33, s[32:33]
	v_cndmask_b32_e64 v34, v38, v34, s[34:35]
	v_cndmask_b32_e64 v35, v39, v35, s[36:37]
	s_add_i32 s22, s23, 40
	s_cmp_lt_i32 s22, s16
	s_cbranch_scc0 .Ln1_skip_10
	s_lshl_b32 s22, s22, 10
	s_add_u32 s26, s12, s22
	s_addc_u32 s27, s13, 0
	global_store_dwordx4 v12, v[32:35], s[26:27] sc1
.Ln1_skip_10:
	s_waitcnt vmcnt(15)
	v_cvt_f32_f16_sdwa v41, v20 dst_sel:DWORD dst_unused:UNUSED_PAD src0_sel:WORD_1
	v_cvt_f32_f16_e32 v40, v20
	v_cvt_f32_f16_sdwa v43, v21 dst_sel:DWORD dst_unused:UNUSED_PAD src0_sel:WORD_1
	v_cvt_f32_f16_e32 v42, v21
	v_pk_fma_f32 v[40:41], v[2:3], v[40:41], v[6:7]
	v_pk_fma_f32 v[42:43], v[4:5], v[42:43], v[8:9]
	v_pk_mul_f32 v[44:45], v[40:41], s[28:29] op_sel_hi:[1,0]
	v_pk_mul_f32 v[46:47], v[42:43], s[28:29] op_sel_hi:[1,0]
	v_cmp_lt_f32_e64 s[30:31], 0, v40
	v_cmp_lt_f32_e64 s[32:33], 0, v41
	v_cmp_lt_f32_e64 s[34:35], 0, v42
	v_cmp_lt_f32_e64 s[36:37], 0, v43
	v_cndmask_b32_e64 v40, v44, v40, s[30:31]
	v_cndmask_b32_e64 v41, v45, v41, s[32:33]
	v_cndmask_b32_e64 v42, v46, v42, s[34:35]
	v_cndmask_b32_e64 v43, v47, v43, s[36:37]
	s_add_i32 s22, s23, 44
	s_cmp_lt_i32 s22, s16
	s_cbranch_scc0 .Ln1_skip_11
	s_lshl_b32 s22, s22, 10
	s_add_u32 s26, s12, s22
	s_addc_u32 s27, s13, 0
	global_store_dwordx4 v12, v[40:43], s[26:27] sc1
.Ln1_skip_11:
	s_waitcnt vmcnt(15)
	v_cvt_f32_f16_sdwa v33, v22 dst_sel:DWORD dst_unused:UNUSED_PAD src0_sel:WORD_1
	v_cvt_f32_f16_e32 v32, v22
	v_cvt_f32_f16_sdwa v35, v23 dst_sel:DWORD dst_unused:UNUSED_PAD src0_sel:WORD_1
	v_cvt_f32_f16_e32 v34, v23
	v_pk_fma_f32 v[32:33], v[2:3], v[32:33], v[6:7]
	v_pk_fma_f32 v[34:35], v[4:5], v[34:35], v[8:9]
	v_pk_mul_f32 v[36:37], v[32:33], s[28:29] op_sel_hi:[1,0]
	v_pk_mul_f32 v[38:39], v[34:35], s[28:29] op_sel_hi:[1,0]
	v_cmp_lt_f32_e64 s[30:31], 0, v32
	v_cmp_lt_f32_e64 s[32:33], 0, v33
	v_cmp_lt_f32_e64 s[34:35], 0, v34
	v_cmp_lt_f32_e64 s[36:37], 0, v35
	v_cndmask_b32_e64 v32, v36, v32, s[30:31]
	v_cndmask_b32_e64 v33, v37, v33, s[32:33]
	v_cndmask_b32_e64 v34, v38, v34, s[34:35]
	v_cndmask_b32_e64 v35, v39, v35, s[36:37]
	s_add_i32 s22, s23, 48
	s_cmp_lt_i32 s22, s16
	s_cbranch_scc0 .Ln1_skip_12
	s_lshl_b32 s22, s22, 10
	s_add_u32 s26, s12, s22
	s_addc_u32 s27, s13, 0
	global_store_dwordx4 v12, v[32:35], s[26:27] sc1
.Ln1_skip_12:
	s_waitcnt vmcnt(15)
	v_cvt_f32_f16_sdwa v41, v24 dst_sel:DWORD dst_unused:UNUSED_PAD src0_sel:WORD_1
	v_cvt_f32_f16_e32 v40, v24
	v_cvt_f32_f16_sdwa v43, v25 dst_sel:DWORD dst_unused:UNUSED_PAD src0_sel:WORD_1
	v_cvt_f32_f16_e32 v42, v25
	v_pk_fma_f32 v[40:41], v[2:3], v[40:41], v[6:7]
	v_pk_fma_f32 v[42:43], v[4:5], v[42:43], v[8:9]
	v_pk_mul_f32 v[44:45], v[40:41], s[28:29] op_sel_hi:[1,0]
	v_pk_mul_f32 v[46:47], v[42:43], s[28:29] op_sel_hi:[1,0]
	v_cmp_lt_f32_e64 s[30:31], 0, v40
	v_cmp_lt_f32_e64 s[32:33], 0, v41
	v_cmp_lt_f32_e64 s[34:35], 0, v42
	v_cmp_lt_f32_e64 s[36:37], 0, v43
	v_cndmask_b32_e64 v40, v44, v40, s[30:31]
	v_cndmask_b32_e64 v41, v45, v41, s[32:33]
	v_cndmask_b32_e64 v42, v46, v42, s[34:35]
	v_cndmask_b32_e64 v43, v47, v43, s[36:37]
	s_add_i32 s22, s23, 52
	s_cmp_lt_i32 s22, s16
	s_cbranch_scc0 .Ln1_skip_13
	s_lshl_b32 s22, s22, 10
	s_add_u32 s26, s12, s22
	s_addc_u32 s27, s13, 0
	global_store_dwordx4 v12, v[40:43], s[26:27] sc1
.Ln1_skip_13:
	s_waitcnt vmcnt(15)
	v_cvt_f32_f16_sdwa v33, v26 dst_sel:DWORD dst_unused:UNUSED_PAD src0_sel:WORD_1
	v_cvt_f32_f16_e32 v32, v26
	v_cvt_f32_f16_sdwa v35, v27 dst_sel:DWORD dst_unused:UNUSED_PAD src0_sel:WORD_1
	v_cvt_f32_f16_e32 v34, v27
	v_pk_fma_f32 v[32:33], v[2:3], v[32:33], v[6:7]
	v_pk_fma_f32 v[34:35], v[4:5], v[34:35], v[8:9]
	v_pk_mul_f32 v[36:37], v[32:33], s[28:29] op_sel_hi:[1,0]
	v_pk_mul_f32 v[38:39], v[34:35], s[28:29] op_sel_hi:[1,0]
	v_cmp_lt_f32_e64 s[30:31], 0, v32
	v_cmp_lt_f32_e64 s[32:33], 0, v33
	v_cmp_lt_f32_e64 s[34:35], 0, v34
	v_cmp_lt_f32_e64 s[36:37], 0, v35
	v_cndmask_b32_e64 v32, v36, v32, s[30:31]
	v_cndmask_b32_e64 v33, v37, v33, s[32:33]
	v_cndmask_b32_e64 v34, v38, v34, s[34:35]
	v_cndmask_b32_e64 v35, v39, v35, s[36:37]
	s_add_i32 s22, s23, 56
	s_cmp_lt_i32 s22, s16
	s_cbranch_scc0 .Ln1_skip_14
	s_lshl_b32 s22, s22, 10
	s_add_u32 s26, s12, s22
	s_addc_u32 s27, s13, 0
	global_store_dwordx4 v12, v[32:35], s[26:27] sc1
.Ln1_skip_14:
	s_waitcnt vmcnt(15)
	v_cvt_f32_f16_sdwa v41, v28 dst_sel:DWORD dst_unused:UNUSED_PAD src0_sel:WORD_1
	v_cvt_f32_f16_e32 v40, v28
	v_cvt_f32_f16_sdwa v43, v29 dst_sel:DWORD dst_unused:UNUSED_PAD src0_sel:WORD_1
	v_cvt_f32_f16_e32 v42, v29
	v_pk_fma_f32 v[40:41], v[2:3], v[40:41], v[6:7]
	v_pk_fma_f32 v[42:43], v[4:5], v[42:43], v[8:9]
	v_pk_mul_f32 v[44:45], v[40:41], s[28:29] op_sel_hi:[1,0]
	v_pk_mul_f32 v[46:47], v[42:43], s[28:29] op_sel_hi:[1,0]
	v_cmp_lt_f32_e64 s[30:31], 0, v40
	v_cmp_lt_f32_e64 s[32:33], 0, v41
	v_cmp_lt_f32_e64 s[34:35], 0, v42
	v_cmp_lt_f32_e64 s[36:37], 0, v43
	v_cndmask_b32_e64 v40, v44, v40, s[30:31]
	v_cndmask_b32_e64 v41, v45, v41, s[32:33]
	v_cndmask_b32_e64 v42, v46, v42, s[34:35]
	v_cndmask_b32_e64 v43, v47, v43, s[36:37]
	s_add_i32 s22, s23, 60
	s_cmp_lt_i32 s22, s16
	s_cbranch_scc0 .Ln1_skip_15
	s_lshl_b32 s22, s22, 10
	s_add_u32 s26, s12, s22
	s_addc_u32 s27, s13, 0
	global_store_dwordx4 v12, v[40:43], s[26:27] sc1

	.amdhsa_kernel _Z6k_normILb1EEvPKDF16_PKdPKfS5_Pvm
		.amdhsa_group_segment_fixed_size 2048
		.amdhsa_private_segment_fixed_size 0
		.amdhsa_kernarg_size 48
		.amdhsa_user_sgpr_count 2
		.amdhsa_user_sgpr_dispatch_ptr 0
		.amdhsa_user_sgpr_queue_ptr 0
		.amdhsa_user_sgpr_kernarg_segment_ptr 1
		.amdhsa_user_sgpr_dispatch_id 0
		.amdhsa_user_sgpr_kernarg_preload_length 0
		.amdhsa_user_sgpr_kernarg_preload_offset 0
		.amdhsa_user_sgpr_private_segment_size 0
		.amdhsa_uses_dynamic_stack 0
		.amdhsa_enable_private_segment 0
		.amdhsa_system_sgpr_workgroup_id_x 1
		.amdhsa_system_sgpr_workgroup_id_y 0
		.amdhsa_system_sgpr_workgroup_id_z 0
		.amdhsa_system_sgpr_workgroup_info 0
		.amdhsa_system_vgpr_workitem_id 0
		.amdhsa_next_free_vgpr 64
		.amdhsa_next_free_sgpr 40
		.amdhsa_accum_offset 64
		.amdhsa_reserve_vcc 1
		.amdhsa_float_round_mode_32 0
		.amdhsa_float_round_mode_16_64 0
		.amdhsa_float_denorm_mode_32 3
		.amdhsa_float_denorm_mode_16_64 3
		.amdhsa_dx10_clamp 1
		.amdhsa_ieee_mode 1
		.amdhsa_fp16_overflow 0
		.amdhsa_tg_split 0
		.amdhsa_exception_fp_ieee_invalid_op 0
		.amdhsa_exception_fp_denorm_src 0
		.amdhsa_exception_fp_ieee_div_zero 0
		.amdhsa_exception_fp_ieee_overflow 0
		.amdhsa_exception_fp_ieee_underflow 0
		.amdhsa_exception_fp_ieee_inexact 0
		.amdhsa_exception_int_div_zero 0
	.end_amdhsa_kernel

amdhsa.kernels:
  - .agpr_count:     0
    .args:
      - .offset:         0
        .size:           336
        .value_kind:     by_value
    .group_segment_fixed_size: 1024
    .kernarg_segment_align: 8
    .kernarg_segment_size: 336
    .language:       OpenCL C
    .language_version:
      - 2
      - 0
    .max_flat_workgroup_size: 256
    .name:           _Z6k_prep8PrepArgs
    .private_segment_fixed_size: 0
    .sgpr_count:     30
    .sgpr_spill_count: 0
    .symbol:         _Z6k_prep8PrepArgs.kd
    .uniform_work_group_size: 1
    .uses_dynamic_stack: false
    .vgpr_count:     20
    .vgpr_spill_count: 0
    .wavefront_size: 64
  - .agpr_count:     0
    .args:
      - .address_space:  global
        .offset:         0
        .size:           8
        .value_kind:     global_buffer
      - .actual_access:  write_only
        .address_space:  global
        .offset:         8
        .size:           8
        .value_kind:     global_buffer
    .group_segment_fixed_size: 16
    .kernarg_segment_align: 8
    .kernarg_segment_size: 16
    .language:       OpenCL C
    .language_version:
      - 2
      - 0
    .max_flat_workgroup_size: 256
    .name:           _Z7k_bscanPiS_
    .private_segment_fixed_size: 0
    .sgpr_count:     22
    .sgpr_spill_count: 0
    .symbol:         _Z7k_bscanPiS_.kd
    .uniform_work_group_size: 1
    .uses_dynamic_stack: false
    .vgpr_count:     18
    .vgpr_spill_count: 0
    .wavefront_size: 64
  - .agpr_count:     16
    .args:
      - .offset:         0
        .size:           24
        .value_kind:     by_value
      - .actual_access:  read_only
        .address_space:  global
        .offset:         24
        .size:           8
        .value_kind:     global_buffer
      - .actual_access:  read_only
        .address_space:  global
        .offset:         32
        .size:           8
        .value_kind:     global_buffer
      - .actual_access:  write_only
        .address_space:  global
        .offset:         40
        .size:           8
        .value_kind:     global_buffer
      - .offset:         48
        .size:           608
        .value_kind:     by_value
      - .actual_access:  read_only
        .address_space:  global
        .offset:         656
        .size:           8
        .value_kind:     global_buffer
      - .actual_access:  write_only
        .address_space:  global
        .offset:         664
        .size:           8
        .value_kind:     global_buffer
    .group_segment_fixed_size: 33024
    .kernarg_segment_align: 8
    .kernarg_segment_size: 672
    .language:       OpenCL C
    .language_version:
      - 2
      - 0
    .max_flat_workgroup_size: 256
    .name:           _Z9k_scatter8EdgePtrsPKiS1_Pj8FoldArgsPKfPDF16_
    .private_segment_fixed_size: 0
    .sgpr_count:     28
    .sgpr_spill_count: 0
    .symbol:         _Z9k_scatter8EdgePtrsPKiS1_Pj8FoldArgsPKfPDF16_.kd
    .uniform_work_group_size: 1
    .uses_dynamic_stack: false
    .vgpr_count:     116
    .vgpr_spill_count: 0
    .wavefront_size: 64
  - .agpr_count:     0
    .args:
      - .actual_access:  read_only
        .address_space:  global
        .offset:         0
        .size:           8
        .value_kind:     global_buffer
      - .actual_access:  read_only
        .address_space:  global
        .offset:         8
        .size:           8
        .value_kind:     global_buffer
      - .actual_access:  write_only
        .address_space:  global
        .offset:         16
        .size:           8
        .value_kind:     global_buffer
      - .actual_access:  write_only
        .address_space:  global
        .offset:         24
        .size:           8
        .value_kind:     global_buffer
      - .actual_access:  read_only
        .address_space:  global
        .offset:         32
        .size:           8
        .value_kind:     global_buffer
      - .actual_access:  write_only
        .address_space:  global
        .offset:         40
        .size:           8
        .value_kind:     global_buffer
    .group_segment_fixed_size: 1048
    .kernarg_segment_align: 8
    .kernarg_segment_size: 48
    .language:       OpenCL C
    .language_version:
      - 2
      - 0
    .max_flat_workgroup_size: 256
    .name:           _Z6k_finePKiPKjPiPtPKfPDF16_
    .private_segment_fixed_size: 0
    .sgpr_count:     47
    .sgpr_spill_count: 0
    .symbol:         _Z6k_finePKiPKjPiPtPKfPDF16_.kd
    .uniform_work_group_size: 1
    .uses_dynamic_stack: false
    .vgpr_count:     28
    .vgpr_spill_count: 0
    .wavefront_size: 64
  - .agpr_count:     0
    .args:
      - .offset:         0
        .size:           40
        .value_kind:     by_value
      - .offset:         40
        .size:           40
        .value_kind:     by_value
      - .offset:         80
        .size:           40
        .value_kind:     by_value
    .group_segment_fixed_size: 0
    .kernarg_segment_align: 8
    .kernarg_segment_size: 120
    .language:       OpenCL C
    .language_version:
      - 2
      - 0
    .max_flat_workgroup_size: 256
    .name:           _Z5k_agg6AggJobS_S_
    .private_segment_fixed_size: 0
    .sgpr_count:     34
    .sgpr_spill_count: 0
    .symbol:         _Z5k_agg6AggJobS_S_.kd
    .uniform_work_group_size: 1
    .uses_dynamic_stack: false
    .vgpr_count:     60
    .vgpr_spill_count: 0
    .wavefront_size: 64
  - .agpr_count:     0
    .args:
      - .offset:         0
        .size:           48
        .value_kind:     by_value
      - .offset:         48
        .size:           48
        .value_kind:     by_value
    .group_segment_fixed_size: 0
    .kernarg_segment_align: 8
    .kernarg_segment_size: 96
    .language:       OpenCL C
    .language_version:
      - 2
      - 0
    .max_flat_workgroup_size: 512
    .name:           _Z6k_gemm8GemmProbS_
    .private_segment_fixed_size: 0
    .sgpr_count:     100
    .sgpr_spill_count: 0
    .symbol:         _Z6k_gemm8GemmProbS_.kd
    .uniform_work_group_size: 1
    .uses_dynamic_stack: false
    .vgpr_count:     240
    .vgpr_spill_count: 0
    .wavefront_size: 64
  - .agpr_count:     0
    .args:
      - .actual_access:  read_only
        .address_space:  global
        .offset:         0
        .size:           8
        .value_kind:     global_buffer
      - .actual_access:  read_only
        .address_space:  global
        .offset:         8
        .size:           8
        .value_kind:     global_buffer
      - .actual_access:  read_only
        .address_space:  global
        .offset:         16
        .size:           8
        .value_kind:     global_buffer
      - .actual_access:  read_only
        .address_space:  global
        .offset:         24
        .size:           8
        .value_kind:     global_buffer
      - .actual_access:  write_only
        .address_space:  global
        .offset:         32
        .size:           8
        .value_kind:     global_buffer
      - .offset:         40
        .size:           8
        .value_kind:     by_value
    .group_segment_fixed_size: 2048
    .kernarg_segment_align: 8
    .kernarg_segment_size: 48
    .language:       OpenCL C
    .language_version:
      - 2
      - 0
    .max_flat_workgroup_size: 256
    .name:           _Z6k_normILb0EEvPKDF16_PKdPKfS5_Pvm
    .private_segment_fixed_size: 0
    .sgpr_count:     23
    .sgpr_spill_count: 0
    .symbol:         _Z6k_normILb0EEvPKDF16_PKdPKfS5_Pvm.kd
    .uniform_work_group_size: 1
    .uses_dynamic_stack: false
    .vgpr_count:     56
    .vgpr_spill_count: 0
    .wavefront_size: 64
  - .agpr_count:     0
    .args:
      - .actual_access:  read_only
        .address_space:  global
        .offset:         0
        .size:           8
        .value_kind:     global_buffer
      - .actual_access:  read_only
        .address_space:  global
        .offset:         8
        .size:           8
        .value_kind:     global_buffer
      - .actual_access:  read_only
        .address_space:  global
        .offset:         16
        .size:           8
        .value_kind:     global_buffer
      - .actual_access:  read_only
        .address_space:  global
        .offset:         24
        .size:           8
        .value_kind:     global_buffer
      - .actual_access:  write_only
        .address_space:  global
        .offset:         32
        .size:           8
        .value_kind:     global_buffer
      - .offset:         40
        .size:           8
        .value_kind:     by_value
    .group_segment_fixed_size: 2048
    .kernarg_segment_align: 8
    .kernarg_segment_size: 48
    .language:       OpenCL C
    .language_version:
      - 2
      - 0
    .max_flat_workgroup_size: 256
    .name:           _Z6k_normILb1EEvPKDF16_PKdPKfS5_Pvm
    .private_segment_fixed_size: 0
    .sgpr_count:     46
    .sgpr_spill_count: 0
    .symbol:         _Z6k_normILb1EEvPKDF16_PKdPKfS5_Pvm.kd
    .uniform_work_group_size: 1
    .uses_dynamic_stack: false
    .vgpr_count:     64
    .vgpr_spill_count: 0
    .wavefront_size: 64
